# ssm_final second-round units re-dealt: blocks 0-127 take 8, blocks 128-255 take 4 (waves 0-3), balancing against the q/k/v GEMM lengths
# baseline (speedup 1.0000x reference)
.LBB0_533:
	v_add_u32_e32 v10, s1, v6
	v_add_u32_e32 v4, 0x10800, v10
	ds_read_b128 v[80:83], v4
	ds_read_b128 v[106:109], v4 offset:16
	v_add_u32_e32 v11, 0x10820, v10
	s_addk_i32 s1, 0x100
	s_cmpk_eq_i32 s1, 0x200
	s_waitcnt lgkmcnt(1)
	v_lshlrev_b32_e32 v4, 16, v80
	v_and_b32_e32 v80, 0xffff0000, v80
	v_lshlrev_b32_e32 v110, 16, v81
	v_and_b32_e32 v112, 0xffff0000, v81
	v_lshlrev_b32_e32 v114, 16, v82
	v_and_b32_e32 v82, 0xffff0000, v82
	v_lshlrev_b32_e32 v116, 16, v83
	v_and_b32_e32 v118, 0xffff0000, v83
	v_pk_fma_f32 v[4:5], v[4:5], v[76:77], 0 op_sel_hi:[0,1,0]
	v_pk_fma_f32 v[80:81], v[80:81], v[56:57], 0 op_sel_hi:[0,1,0]
	v_pk_fma_f32 v[110:111], v[110:111], v[60:61], 0 op_sel_hi:[0,1,0]
	v_pk_fma_f32 v[112:113], v[112:113], v[58:59], 0 op_sel_hi:[0,1,0]
	s_waitcnt lgkmcnt(0)
	v_lshlrev_b32_e32 v120, 16, v106
	v_and_b32_e32 v106, 0xffff0000, v106
	v_lshlrev_b32_e32 v122, 16, v107
	v_and_b32_e32 v124, 0xffff0000, v107
	v_pk_fma_f32 v[4:5], v[114:115], v[62:63], v[4:5] op_sel_hi:[0,1,1]
	v_pk_fma_f32 v[80:81], v[82:83], v[48:49], v[80:81] op_sel_hi:[0,1,1]
	v_pk_fma_f32 v[82:83], v[116:117], v[52:53], v[110:111] op_sel_hi:[0,1,1]
	v_pk_fma_f32 v[110:111], v[118:119], v[50:51], v[112:113] op_sel_hi:[0,1,1]
	v_lshlrev_b32_e32 v126, 16, v108
	v_and_b32_e32 v108, 0xffff0000, v108
	v_lshlrev_b32_e32 v128, 16, v109
	v_and_b32_e32 v130, 0xffff0000, v109
	v_pk_fma_f32 v[4:5], v[120:121], v[54:55], v[4:5] op_sel_hi:[0,1,1]
	v_pk_fma_f32 v[80:81], v[106:107], v[40:41], v[80:81] op_sel_hi:[0,1,1]
	v_pk_fma_f32 v[82:83], v[122:123], v[44:45], v[82:83] op_sel_hi:[0,1,1]
	v_pk_fma_f32 v[106:107], v[124:125], v[42:43], v[110:111] op_sel_hi:[0,1,1]
	v_pk_fma_f32 v[4:5], v[126:127], v[46:47], v[4:5] op_sel_hi:[0,1,1]
	v_pk_fma_f32 v[80:81], v[108:109], v[24:25], v[80:81] op_sel_hi:[0,1,1]
	v_pk_fma_f32 v[82:83], v[128:129], v[36:37], v[82:83] op_sel_hi:[0,1,1]
	v_pk_fma_f32 v[106:107], v[130:131], v[26:27], v[106:107] op_sel_hi:[0,1,1]
	v_pk_add_f32 v[4:5], v[4:5], v[80:81]
	v_pk_add_f32 v[80:81], v[82:83], v[106:107]
	s_nop 0
	v_pk_add_f32 v[4:5], v[4:5], v[80:81]
	s_nop 0
	v_pk_fma_f32 v[4:5], v[74:75], v[78:79], v[4:5] op_sel:[0,1,0] op_sel_hi:[1,0,1]
	s_nop 0
	v_pk_fma_f32 v[4:5], v[72:73], v[78:79], v[4:5]
	ds_write2st64_b32 v7, v5, v4 offset1:1
	ds_read_b128 v[78:81], v11
	ds_read_b128 v[106:109], v11 offset:16
	v_add_u32_e32 v11, 0x10840, v10
	s_waitcnt lgkmcnt(1)
	v_lshlrev_b32_e32 v82, 16, v78
	v_and_b32_e32 v78, 0xffff0000, v78
	v_lshlrev_b32_e32 v110, 16, v79
	v_and_b32_e32 v112, 0xffff0000, v79
	v_lshlrev_b32_e32 v114, 16, v80
	v_and_b32_e32 v80, 0xffff0000, v80
	v_lshlrev_b32_e32 v116, 16, v81
	v_and_b32_e32 v118, 0xffff0000, v81
	v_pk_fma_f32 v[82:83], v[82:83], v[76:77], 0 op_sel_hi:[0,1,0]
	v_pk_fma_f32 v[78:79], v[78:79], v[56:57], 0 op_sel_hi:[0,1,0]
	v_pk_fma_f32 v[110:111], v[110:111], v[60:61], 0 op_sel_hi:[0,1,0]
	v_pk_fma_f32 v[112:113], v[112:113], v[58:59], 0 op_sel_hi:[0,1,0]
	s_waitcnt lgkmcnt(0)
	v_lshlrev_b32_e32 v120, 16, v106
	v_and_b32_e32 v106, 0xffff0000, v106
	v_lshlrev_b32_e32 v122, 16, v107
	v_and_b32_e32 v124, 0xffff0000, v107
	v_pk_fma_f32 v[82:83], v[114:115], v[62:63], v[82:83] op_sel_hi:[0,1,1]
	v_pk_fma_f32 v[78:79], v[80:81], v[48:49], v[78:79] op_sel_hi:[0,1,1]
	v_pk_fma_f32 v[80:81], v[116:117], v[52:53], v[110:111] op_sel_hi:[0,1,1]
	v_pk_fma_f32 v[110:111], v[118:119], v[50:51], v[112:113] op_sel_hi:[0,1,1]
	v_lshlrev_b32_e32 v126, 16, v108
	v_and_b32_e32 v108, 0xffff0000, v108
	v_lshlrev_b32_e32 v128, 16, v109
	v_and_b32_e32 v130, 0xffff0000, v109
	v_pk_fma_f32 v[82:83], v[120:121], v[54:55], v[82:83] op_sel_hi:[0,1,1]
	v_pk_fma_f32 v[78:79], v[106:107], v[40:41], v[78:79] op_sel_hi:[0,1,1]
	v_pk_fma_f32 v[80:81], v[122:123], v[44:45], v[80:81] op_sel_hi:[0,1,1]
	v_pk_fma_f32 v[106:107], v[124:125], v[42:43], v[110:111] op_sel_hi:[0,1,1]
	v_pk_fma_f32 v[82:83], v[126:127], v[46:47], v[82:83] op_sel_hi:[0,1,1]
	v_pk_fma_f32 v[78:79], v[108:109], v[24:25], v[78:79] op_sel_hi:[0,1,1]
	v_pk_fma_f32 v[80:81], v[128:129], v[36:37], v[80:81] op_sel_hi:[0,1,1]
	v_pk_fma_f32 v[106:107], v[130:131], v[26:27], v[106:107] op_sel_hi:[0,1,1]
	v_pk_add_f32 v[78:79], v[82:83], v[78:79]
	v_pk_add_f32 v[80:81], v[80:81], v[106:107]
	s_nop 0
	v_pk_add_f32 v[78:79], v[78:79], v[80:81]
	s_nop 0
	v_pk_fma_f32 v[78:79], v[74:75], v[4:5], v[78:79] op_sel:[0,1,0] op_sel_hi:[1,0,1]
	s_nop 0
	v_pk_fma_f32 v[4:5], v[72:73], v[4:5], v[78:79]
	ds_write2_b32 v7, v5, v4 offset0:132 offset1:196
	ds_read_b128 v[78:81], v11
	ds_read_b128 v[106:109], v11 offset:16
	v_add_u32_e32 v11, 32, v7
	s_waitcnt lgkmcnt(1)
	v_lshlrev_b32_e32 v82, 16, v78
	v_and_b32_e32 v78, 0xffff0000, v78
	v_lshlrev_b32_e32 v110, 16, v79
	v_and_b32_e32 v112, 0xffff0000, v79
	v_lshlrev_b32_e32 v114, 16, v80
	v_and_b32_e32 v80, 0xffff0000, v80
	v_lshlrev_b32_e32 v116, 16, v81
	v_and_b32_e32 v118, 0xffff0000, v81
	v_pk_fma_f32 v[82:83], v[82:83], v[76:77], 0 op_sel_hi:[0,1,0]
	v_pk_fma_f32 v[78:79], v[78:79], v[56:57], 0 op_sel_hi:[0,1,0]
	v_pk_fma_f32 v[110:111], v[110:111], v[60:61], 0 op_sel_hi:[0,1,0]
	v_pk_fma_f32 v[112:113], v[112:113], v[58:59], 0 op_sel_hi:[0,1,0]
	s_waitcnt lgkmcnt(0)
	v_lshlrev_b32_e32 v120, 16, v106
	v_and_b32_e32 v106, 0xffff0000, v106
	v_lshlrev_b32_e32 v122, 16, v107
	v_and_b32_e32 v124, 0xffff0000, v107
	v_pk_fma_f32 v[82:83], v[114:115], v[62:63], v[82:83] op_sel_hi:[0,1,1]
	v_pk_fma_f32 v[78:79], v[80:81], v[48:49], v[78:79] op_sel_hi:[0,1,1]
	v_pk_fma_f32 v[80:81], v[116:117], v[52:53], v[110:111] op_sel_hi:[0,1,1]
	v_pk_fma_f32 v[110:111], v[118:119], v[50:51], v[112:113] op_sel_hi:[0,1,1]
	v_lshlrev_b32_e32 v126, 16, v108
	v_and_b32_e32 v108, 0xffff0000, v108
	v_lshlrev_b32_e32 v128, 16, v109
	v_and_b32_e32 v130, 0xffff0000, v109
	v_pk_fma_f32 v[82:83], v[120:121], v[54:55], v[82:83] op_sel_hi:[0,1,1]
	v_pk_fma_f32 v[78:79], v[106:107], v[40:41], v[78:79] op_sel_hi:[0,1,1]
	v_pk_fma_f32 v[80:81], v[122:123], v[44:45], v[80:81] op_sel_hi:[0,1,1]
	v_pk_fma_f32 v[106:107], v[124:125], v[42:43], v[110:111] op_sel_hi:[0,1,1]
	v_pk_fma_f32 v[82:83], v[126:127], v[46:47], v[82:83] op_sel_hi:[0,1,1]
	v_pk_fma_f32 v[78:79], v[108:109], v[24:25], v[78:79] op_sel_hi:[0,1,1]
	v_pk_fma_f32 v[80:81], v[128:129], v[36:37], v[80:81] op_sel_hi:[0,1,1]
	v_pk_fma_f32 v[106:107], v[130:131], v[26:27], v[106:107] op_sel_hi:[0,1,1]
	v_pk_add_f32 v[78:79], v[82:83], v[78:79]
	v_pk_add_f32 v[80:81], v[80:81], v[106:107]
	s_nop 0
	v_pk_add_f32 v[78:79], v[78:79], v[80:81]
	s_nop 0
	v_pk_fma_f32 v[78:79], v[74:75], v[4:5], v[78:79] op_sel:[0,1,0] op_sel_hi:[1,0,1]
	s_nop 0
	v_pk_fma_f32 v[4:5], v[72:73], v[4:5], v[78:79]
	ds_write2st64_b32 v11, v5, v4 offset0:4 offset1:5
	v_add_u32_e32 v11, 0x10860, v10
	ds_read_b128 v[78:81], v11
	ds_read_b128 v[106:109], v11 offset:16
	v_add_u32_e32 v11, 48, v7
	s_waitcnt lgkmcnt(1)
	v_lshlrev_b32_e32 v82, 16, v78
	v_and_b32_e32 v78, 0xffff0000, v78
	v_lshlrev_b32_e32 v110, 16, v79
	v_and_b32_e32 v112, 0xffff0000, v79
	v_lshlrev_b32_e32 v114, 16, v80
	v_and_b32_e32 v80, 0xffff0000, v80
	v_lshlrev_b32_e32 v116, 16, v81
	v_and_b32_e32 v118, 0xffff0000, v81
	v_pk_fma_f32 v[82:83], v[82:83], v[76:77], 0 op_sel_hi:[0,1,0]
	v_pk_fma_f32 v[78:79], v[78:79], v[56:57], 0 op_sel_hi:[0,1,0]
	v_pk_fma_f32 v[110:111], v[110:111], v[60:61], 0 op_sel_hi:[0,1,0]
	v_pk_fma_f32 v[112:113], v[112:113], v[58:59], 0 op_sel_hi:[0,1,0]
	s_waitcnt lgkmcnt(0)
	v_lshlrev_b32_e32 v120, 16, v106
	v_and_b32_e32 v106, 0xffff0000, v106
	v_lshlrev_b32_e32 v122, 16, v107
	v_and_b32_e32 v124, 0xffff0000, v107
	v_pk_fma_f32 v[82:83], v[114:115], v[62:63], v[82:83] op_sel_hi:[0,1,1]
	v_pk_fma_f32 v[78:79], v[80:81], v[48:49], v[78:79] op_sel_hi:[0,1,1]
	v_pk_fma_f32 v[80:81], v[116:117], v[52:53], v[110:111] op_sel_hi:[0,1,1]
	v_pk_fma_f32 v[110:111], v[118:119], v[50:51], v[112:113] op_sel_hi:[0,1,1]
	v_lshlrev_b32_e32 v126, 16, v108
	v_and_b32_e32 v108, 0xffff0000, v108
	v_lshlrev_b32_e32 v128, 16, v109
	v_and_b32_e32 v130, 0xffff0000, v109
	v_pk_fma_f32 v[82:83], v[120:121], v[54:55], v[82:83] op_sel_hi:[0,1,1]
	v_pk_fma_f32 v[78:79], v[106:107], v[40:41], v[78:79] op_sel_hi:[0,1,1]
	v_pk_fma_f32 v[80:81], v[122:123], v[44:45], v[80:81] op_sel_hi:[0,1,1]
	v_pk_fma_f32 v[106:107], v[124:125], v[42:43], v[110:111] op_sel_hi:[0,1,1]
	v_pk_fma_f32 v[82:83], v[126:127], v[46:47], v[82:83] op_sel_hi:[0,1,1]
	v_pk_fma_f32 v[78:79], v[108:109], v[24:25], v[78:79] op_sel_hi:[0,1,1]
	v_pk_fma_f32 v[80:81], v[128:129], v[36:37], v[80:81] op_sel_hi:[0,1,1]
	v_pk_fma_f32 v[106:107], v[130:131], v[26:27], v[106:107] op_sel_hi:[0,1,1]
	v_pk_add_f32 v[78:79], v[82:83], v[78:79]
	v_pk_add_f32 v[80:81], v[80:81], v[106:107]
	s_nop 0
	v_pk_add_f32 v[78:79], v[78:79], v[80:81]
	s_nop 0
	v_pk_fma_f32 v[78:79], v[74:75], v[4:5], v[78:79] op_sel:[0,1,0] op_sel_hi:[1,0,1]
	s_nop 0
	v_pk_fma_f32 v[4:5], v[72:73], v[4:5], v[78:79]
	ds_write2st64_b32 v11, v5, v4 offset0:6 offset1:7
	v_add_u32_e32 v11, 0x10880, v10
	ds_read_b128 v[78:81], v11
	ds_read_b128 v[106:109], v11 offset:16
	v_add_u32_e32 v11, 64, v7
	s_waitcnt lgkmcnt(1)
	v_lshlrev_b32_e32 v82, 16, v78
	v_and_b32_e32 v78, 0xffff0000, v78
	v_lshlrev_b32_e32 v110, 16, v79
	v_and_b32_e32 v112, 0xffff0000, v79
	v_lshlrev_b32_e32 v114, 16, v80
	v_and_b32_e32 v80, 0xffff0000, v80
	v_lshlrev_b32_e32 v116, 16, v81
	v_and_b32_e32 v118, 0xffff0000, v81
	v_pk_fma_f32 v[82:83], v[82:83], v[76:77], 0 op_sel_hi:[0,1,0]
	v_pk_fma_f32 v[78:79], v[78:79], v[56:57], 0 op_sel_hi:[0,1,0]
	v_pk_fma_f32 v[110:111], v[110:111], v[60:61], 0 op_sel_hi:[0,1,0]
	v_pk_fma_f32 v[112:113], v[112:113], v[58:59], 0 op_sel_hi:[0,1,0]
	s_waitcnt lgkmcnt(0)
	v_lshlrev_b32_e32 v120, 16, v106
	v_and_b32_e32 v106, 0xffff0000, v106
	v_lshlrev_b32_e32 v122, 16, v107
	v_and_b32_e32 v124, 0xffff0000, v107
	v_pk_fma_f32 v[82:83], v[114:115], v[62:63], v[82:83] op_sel_hi:[0,1,1]
	v_pk_fma_f32 v[78:79], v[80:81], v[48:49], v[78:79] op_sel_hi:[0,1,1]
	v_pk_fma_f32 v[80:81], v[116:117], v[52:53], v[110:111] op_sel_hi:[0,1,1]
	v_pk_fma_f32 v[110:111], v[118:119], v[50:51], v[112:113] op_sel_hi:[0,1,1]
	v_lshlrev_b32_e32 v126, 16, v108
	v_and_b32_e32 v108, 0xffff0000, v108
	v_lshlrev_b32_e32 v128, 16, v109
	v_and_b32_e32 v130, 0xffff0000, v109
	v_pk_fma_f32 v[82:83], v[120:121], v[54:55], v[82:83] op_sel_hi:[0,1,1]
	v_pk_fma_f32 v[78:79], v[106:107], v[40:41], v[78:79] op_sel_hi:[0,1,1]
	v_pk_fma_f32 v[80:81], v[122:123], v[44:45], v[80:81] op_sel_hi:[0,1,1]
	v_pk_fma_f32 v[106:107], v[124:125], v[42:43], v[110:111] op_sel_hi:[0,1,1]
	v_pk_fma_f32 v[82:83], v[126:127], v[46:47], v[82:83] op_sel_hi:[0,1,1]
	v_pk_fma_f32 v[78:79], v[108:109], v[24:25], v[78:79] op_sel_hi:[0,1,1]
	v_pk_fma_f32 v[80:81], v[128:129], v[36:37], v[80:81] op_sel_hi:[0,1,1]
	v_pk_fma_f32 v[106:107], v[130:131], v[26:27], v[106:107] op_sel_hi:[0,1,1]
	v_pk_add_f32 v[78:79], v[82:83], v[78:79]
	v_pk_add_f32 v[80:81], v[80:81], v[106:107]
	s_nop 0
	v_pk_add_f32 v[78:79], v[78:79], v[80:81]
	s_nop 0
	v_pk_fma_f32 v[78:79], v[74:75], v[4:5], v[78:79] op_sel:[0,1,0] op_sel_hi:[1,0,1]
	s_nop 0
	v_pk_fma_f32 v[4:5], v[72:73], v[4:5], v[78:79]
	ds_write2st64_b32 v11, v5, v4 offset0:8 offset1:9
	v_add_u32_e32 v11, 0x108a0, v10
	ds_read_b128 v[78:81], v11
	ds_read_b128 v[106:109], v11 offset:16
	v_add_u32_e32 v11, 0x50, v7
	s_waitcnt lgkmcnt(1)
	v_lshlrev_b32_e32 v82, 16, v78
	v_and_b32_e32 v78, 0xffff0000, v78
	v_lshlrev_b32_e32 v110, 16, v79
	v_and_b32_e32 v112, 0xffff0000, v79
	v_lshlrev_b32_e32 v114, 16, v80
	v_and_b32_e32 v80, 0xffff0000, v80
	v_lshlrev_b32_e32 v116, 16, v81
	v_and_b32_e32 v118, 0xffff0000, v81
	v_pk_fma_f32 v[82:83], v[82:83], v[76:77], 0 op_sel_hi:[0,1,0]
	v_pk_fma_f32 v[78:79], v[78:79], v[56:57], 0 op_sel_hi:[0,1,0]
	v_pk_fma_f32 v[110:111], v[110:111], v[60:61], 0 op_sel_hi:[0,1,0]
	v_pk_fma_f32 v[112:113], v[112:113], v[58:59], 0 op_sel_hi:[0,1,0]
	s_waitcnt lgkmcnt(0)
	v_lshlrev_b32_e32 v120, 16, v106
	v_and_b32_e32 v106, 0xffff0000, v106
	v_lshlrev_b32_e32 v122, 16, v107
	v_and_b32_e32 v124, 0xffff0000, v107
	v_pk_fma_f32 v[82:83], v[114:115], v[62:63], v[82:83] op_sel_hi:[0,1,1]
	v_pk_fma_f32 v[78:79], v[80:81], v[48:49], v[78:79] op_sel_hi:[0,1,1]
	v_pk_fma_f32 v[80:81], v[116:117], v[52:53], v[110:111] op_sel_hi:[0,1,1]
	v_pk_fma_f32 v[110:111], v[118:119], v[50:51], v[112:113] op_sel_hi:[0,1,1]
	v_lshlrev_b32_e32 v126, 16, v108
	v_and_b32_e32 v108, 0xffff0000, v108
	v_lshlrev_b32_e32 v128, 16, v109
	v_and_b32_e32 v130, 0xffff0000, v109
	v_pk_fma_f32 v[82:83], v[120:121], v[54:55], v[82:83] op_sel_hi:[0,1,1]
	v_pk_fma_f32 v[78:79], v[106:107], v[40:41], v[78:79] op_sel_hi:[0,1,1]
	v_pk_fma_f32 v[80:81], v[122:123], v[44:45], v[80:81] op_sel_hi:[0,1,1]
	v_pk_fma_f32 v[106:107], v[124:125], v[42:43], v[110:111] op_sel_hi:[0,1,1]
	v_pk_fma_f32 v[82:83], v[126:127], v[46:47], v[82:83] op_sel_hi:[0,1,1]
	v_pk_fma_f32 v[78:79], v[108:109], v[24:25], v[78:79] op_sel_hi:[0,1,1]
	v_pk_fma_f32 v[80:81], v[128:129], v[36:37], v[80:81] op_sel_hi:[0,1,1]
	v_pk_fma_f32 v[106:107], v[130:131], v[26:27], v[106:107] op_sel_hi:[0,1,1]
	v_pk_add_f32 v[78:79], v[82:83], v[78:79]
	v_pk_add_f32 v[80:81], v[80:81], v[106:107]
	s_nop 0
	v_pk_add_f32 v[78:79], v[78:79], v[80:81]
	s_nop 0
	v_pk_fma_f32 v[78:79], v[74:75], v[4:5], v[78:79] op_sel:[0,1,0] op_sel_hi:[1,0,1]
	s_nop 0
	v_pk_fma_f32 v[4:5], v[72:73], v[4:5], v[78:79]
	ds_write2st64_b32 v11, v5, v4 offset0:10 offset1:11
	v_add_u32_e32 v11, 0x108c0, v10
	ds_read_b128 v[78:81], v11
	ds_read_b128 v[106:109], v11 offset:16
	v_add_u32_e32 v11, 0x60, v7
	v_add_u32_e32 v10, 0x108e0, v10
	s_waitcnt lgkmcnt(1)
	v_lshlrev_b32_e32 v82, 16, v78
	v_and_b32_e32 v78, 0xffff0000, v78
	v_lshlrev_b32_e32 v110, 16, v79
	v_and_b32_e32 v112, 0xffff0000, v79
	v_lshlrev_b32_e32 v114, 16, v80
	v_and_b32_e32 v80, 0xffff0000, v80
	v_lshlrev_b32_e32 v116, 16, v81
	v_and_b32_e32 v118, 0xffff0000, v81
	v_pk_fma_f32 v[82:83], v[82:83], v[76:77], 0 op_sel_hi:[0,1,0]
	v_pk_fma_f32 v[78:79], v[78:79], v[56:57], 0 op_sel_hi:[0,1,0]
	v_pk_fma_f32 v[110:111], v[110:111], v[60:61], 0 op_sel_hi:[0,1,0]
	v_pk_fma_f32 v[112:113], v[112:113], v[58:59], 0 op_sel_hi:[0,1,0]
	s_waitcnt lgkmcnt(0)
	v_lshlrev_b32_e32 v120, 16, v106
	v_and_b32_e32 v106, 0xffff0000, v106
	v_lshlrev_b32_e32 v122, 16, v107
	v_and_b32_e32 v124, 0xffff0000, v107
	v_pk_fma_f32 v[82:83], v[114:115], v[62:63], v[82:83] op_sel_hi:[0,1,1]
	v_pk_fma_f32 v[78:79], v[80:81], v[48:49], v[78:79] op_sel_hi:[0,1,1]
	v_pk_fma_f32 v[80:81], v[116:117], v[52:53], v[110:111] op_sel_hi:[0,1,1]
	v_pk_fma_f32 v[110:111], v[118:119], v[50:51], v[112:113] op_sel_hi:[0,1,1]
	v_lshlrev_b32_e32 v126, 16, v108
	v_and_b32_e32 v108, 0xffff0000, v108
	v_lshlrev_b32_e32 v128, 16, v109
	v_and_b32_e32 v130, 0xffff0000, v109
	v_pk_fma_f32 v[82:83], v[120:121], v[54:55], v[82:83] op_sel_hi:[0,1,1]
	v_pk_fma_f32 v[78:79], v[106:107], v[40:41], v[78:79] op_sel_hi:[0,1,1]
	v_pk_fma_f32 v[80:81], v[122:123], v[44:45], v[80:81] op_sel_hi:[0,1,1]
	v_pk_fma_f32 v[106:107], v[124:125], v[42:43], v[110:111] op_sel_hi:[0,1,1]
	v_pk_fma_f32 v[82:83], v[126:127], v[46:47], v[82:83] op_sel_hi:[0,1,1]
	v_pk_fma_f32 v[78:79], v[108:109], v[24:25], v[78:79] op_sel_hi:[0,1,1]
	v_pk_fma_f32 v[80:81], v[128:129], v[36:37], v[80:81] op_sel_hi:[0,1,1]
	v_pk_fma_f32 v[106:107], v[130:131], v[26:27], v[106:107] op_sel_hi:[0,1,1]
	v_pk_add_f32 v[78:79], v[82:83], v[78:79]
	v_pk_add_f32 v[80:81], v[80:81], v[106:107]
	s_nop 0
	v_pk_add_f32 v[78:79], v[78:79], v[80:81]
	s_nop 0
	v_pk_fma_f32 v[78:79], v[74:75], v[4:5], v[78:79] op_sel:[0,1,0] op_sel_hi:[1,0,1]
	s_nop 0
	v_pk_fma_f32 v[4:5], v[72:73], v[4:5], v[78:79]
	ds_write2st64_b32 v11, v5, v4 offset0:12 offset1:13
	ds_read_b128 v[78:81], v10
	ds_read_b128 v[106:109], v10 offset:16
	s_waitcnt lgkmcnt(1)
	v_lshlrev_b32_e32 v10, 16, v78
	v_and_b32_e32 v78, 0xffff0000, v78
	v_lshlrev_b32_e32 v82, 16, v79
	v_and_b32_e32 v110, 0xffff0000, v79
	v_lshlrev_b32_e32 v112, 16, v80
	v_and_b32_e32 v80, 0xffff0000, v80
	v_lshlrev_b32_e32 v114, 16, v81
	v_and_b32_e32 v116, 0xffff0000, v81
	v_pk_fma_f32 v[10:11], v[10:11], v[76:77], 0 op_sel_hi:[0,1,0]
	v_pk_fma_f32 v[78:79], v[78:79], v[56:57], 0 op_sel_hi:[0,1,0]
	v_pk_fma_f32 v[82:83], v[82:83], v[60:61], 0 op_sel_hi:[0,1,0]
	v_pk_fma_f32 v[110:111], v[110:111], v[58:59], 0 op_sel_hi:[0,1,0]
	s_waitcnt lgkmcnt(0)
	v_lshlrev_b32_e32 v118, 16, v106
	v_and_b32_e32 v106, 0xffff0000, v106
	v_lshlrev_b32_e32 v120, 16, v107
	v_and_b32_e32 v122, 0xffff0000, v107
	v_pk_fma_f32 v[10:11], v[112:113], v[62:63], v[10:11] op_sel_hi:[0,1,1]
	v_pk_fma_f32 v[78:79], v[80:81], v[48:49], v[78:79] op_sel_hi:[0,1,1]
	v_pk_fma_f32 v[80:81], v[114:115], v[52:53], v[82:83] op_sel_hi:[0,1,1]
	v_pk_fma_f32 v[82:83], v[116:117], v[50:51], v[110:111] op_sel_hi:[0,1,1]
	v_lshlrev_b32_e32 v124, 16, v108
	v_and_b32_e32 v108, 0xffff0000, v108
	v_lshlrev_b32_e32 v126, 16, v109
	v_and_b32_e32 v128, 0xffff0000, v109
	v_pk_fma_f32 v[10:11], v[118:119], v[54:55], v[10:11] op_sel_hi:[0,1,1]
	v_pk_fma_f32 v[78:79], v[106:107], v[40:41], v[78:79] op_sel_hi:[0,1,1]
	v_pk_fma_f32 v[80:81], v[120:121], v[44:45], v[80:81] op_sel_hi:[0,1,1]
	v_pk_fma_f32 v[82:83], v[122:123], v[42:43], v[82:83] op_sel_hi:[0,1,1]
	v_pk_fma_f32 v[10:11], v[124:125], v[46:47], v[10:11] op_sel_hi:[0,1,1]
	v_pk_fma_f32 v[78:79], v[108:109], v[24:25], v[78:79] op_sel_hi:[0,1,1]
	v_pk_fma_f32 v[80:81], v[126:127], v[36:37], v[80:81] op_sel_hi:[0,1,1]
	v_pk_fma_f32 v[82:83], v[128:129], v[26:27], v[82:83] op_sel_hi:[0,1,1]
	v_pk_add_f32 v[10:11], v[10:11], v[78:79]
	v_pk_add_f32 v[78:79], v[80:81], v[82:83]
	s_nop 0
	v_pk_add_f32 v[10:11], v[10:11], v[78:79]
	s_nop 0
	v_pk_fma_f32 v[10:11], v[74:75], v[4:5], v[10:11] op_sel:[0,1,0] op_sel_hi:[1,0,1]
	s_nop 0
	v_pk_fma_f32 v[78:79], v[72:73], v[4:5], v[10:11]
	v_add_u32_e32 v4, 0x70, v7
	v_add_u32_e32 v7, 0x1080, v7
	ds_write2st64_b32 v4, v79, v78 offset0:14 offset1:15
	s_cbranch_scc0 .LBB0_533
	s_waitcnt lgkmcnt(0)
	ds_read_b128 v[80:83], v99
	ds_read_b128 v[106:109], v99 offset:16
	v_lshl_or_b32 v7, s0, 4, v95
	v_or_b32_e32 v4, v8, v7
	v_lshl_add_u32 v10, v7, 5, v96
	s_waitcnt lgkmcnt(1)
	v_mfma_f32_16x16x4_f32 v[110:113], v80, v32, 0
	v_or_b32_e32 v71, 1, v7
	v_or_b32_e32 v105, 2, v7
	v_or_b32_e32 v7, 3, v7
	v_or_b32_e32 v114, v8, v105
	v_lshl_add_u32 v105, v105, 5, v96
	v_or_b32_e32 v116, v8, v7
	v_lshl_add_u32 v7, v7, 5, v96
	v_mfma_f32_16x16x4_f32 v[110:113], v81, v33, v[110:113]
	v_mov_b32_e32 v5, v9
	v_mov_b32_e32 v11, v9
	v_mov_b32_e32 v115, v9
	v_mov_b32_e32 v117, v9
	s_add_i32 s0, s0, 1
	v_mad_u64_u32 v[118:119], s[4:5], v114, s95, v[0:1]
	v_mfma_f32_16x16x4_f32 v[110:113], v82, v34, v[110:113]
	s_cmp_eq_u32 s0, 4
	v_lshlrev_b64 v[114:115], 10, v[114:115]
	v_mad_i32_i24 v119, v9, s95, v119
	v_add_u32_e32 v6, 0x200, v6
	v_lshl_add_u64 v[114:115], v[2:3], 0, v[114:115]
	v_mfma_f32_16x16x4_f32 v[80:83], v83, v35, v[110:113]
	s_waitcnt lgkmcnt(0)
	v_mfma_f32_16x16x4_f32 v[80:83], v106, v28, v[80:83]
	v_mfma_f32_16x16x4_f32 v[80:83], v107, v29, v[80:83]
	v_mfma_f32_16x16x4_f32 v[80:83], v108, v30, v[80:83]
	v_mfma_f32_16x16x4_f32 v[80:83], v109, v31, v[80:83]
	ds_read_b128 v[106:109], v99 offset:32
	ds_read_b128 v[110:113], v99 offset:48
	s_waitcnt lgkmcnt(1)
	v_mfma_f32_16x16x4_f32 v[80:83], v106, v20, v[80:83]
	v_mfma_f32_16x16x4_f32 v[80:83], v107, v21, v[80:83]
	v_mfma_f32_16x16x4_f32 v[80:83], v108, v22, v[80:83]
	v_mfma_f32_16x16x4_f32 v[80:83], v109, v23, v[80:83]
	s_waitcnt lgkmcnt(0)
	v_mfma_f32_16x16x4_f32 v[80:83], v110, v16, v[80:83]
	v_mfma_f32_16x16x4_f32 v[80:83], v111, v17, v[80:83]
	v_mfma_f32_16x16x4_f32 v[80:83], v112, v18, v[80:83]
	v_mfma_f32_16x16x4_f32 v[80:83], v113, v19, v[80:83]
	ds_read_b128 v[106:109], v99 offset:64
	ds_read_b128 v[110:113], v99 offset:80
	s_waitcnt lgkmcnt(1)
	v_mfma_f32_16x16x4_f32 v[80:83], v106, v12, v[80:83]
	v_mfma_f32_16x16x4_f32 v[80:83], v107, v13, v[80:83]
	v_mfma_f32_16x16x4_f32 v[80:83], v108, v14, v[80:83]
	v_mfma_f32_16x16x4_f32 v[80:83], v109, v15, v[80:83]
	s_waitcnt lgkmcnt(0)
	v_mfma_f32_16x16x4_f32 v[80:83], v110, v38, v[80:83]
	v_mfma_f32_16x16x4_f32 v[80:83], v111, v39, v[80:83]
	v_mfma_f32_16x16x4_f32 v[80:83], v112, v84, v[80:83]
	v_mfma_f32_16x16x4_f32 v[80:83], v113, v85, v[80:83]
	ds_read_b128 v[106:109], v99 offset:96
	ds_read_b128 v[110:113], v99 offset:112
	s_waitcnt lgkmcnt(0)
	ds_read_u16 v120, v10
	v_or_b32_e32 v10, v8, v71
	v_lshl_add_u32 v71, v71, 5, v96
	ds_read_u16 v71, v71
	ds_read_u16 v105, v105
	s_waitcnt lgkmcnt(4)
	v_mfma_f32_16x16x4_f32 v[80:83], v106, v86, v[80:83]
	ds_read_u16 v7, v7
	s_waitcnt lgkmcnt(2)
	v_lshlrev_b32_e32 v71, 16, v71
	s_waitcnt lgkmcnt(1)
	v_lshlrev_b32_e32 v105, 16, v105
	s_waitcnt lgkmcnt(0)
	v_lshlrev_b32_e32 v7, 16, v7
	v_mfma_f32_16x16x4_f32 v[80:83], v107, v87, v[80:83]
	v_mad_u64_u32 v[106:107], s[4:5], v4, s95, v[0:1]
	v_lshlrev_b64 v[4:5], 10, v[4:5]
	v_mad_i32_i24 v107, v9, s95, v107
	v_lshl_add_u64 v[4:5], v[2:3], 0, v[4:5]
	v_mfma_f32_16x16x4_f32 v[80:83], v108, v88, v[80:83]
	v_mfma_f32_16x16x4_f32 v[80:83], v109, v89, v[80:83]
	v_mad_u64_u32 v[108:109], s[4:5], v10, s95, v[0:1]
	v_lshlrev_b64 v[10:11], 10, v[10:11]
	v_mad_i32_i24 v109, v9, s95, v109
	v_lshl_add_u64 v[10:11], v[2:3], 0, v[10:11]
	v_mfma_f32_16x16x4_f32 v[80:83], v110, v101, v[80:83]
	v_mfma_f32_16x16x4_f32 v[80:83], v111, v102, v[80:83]
	v_mad_u64_u32 v[110:111], s[4:5], v116, s95, v[0:1]
	v_lshlrev_b64 v[116:117], 10, v[116:117]
	v_mad_i32_i24 v111, v9, s95, v111
	v_lshl_add_u64 v[116:117], v[2:3], 0, v[116:117]
	v_mfma_f32_16x16x4_f32 v[80:83], v112, v103, v[80:83]
	v_lshlrev_b32_e32 v112, 16, v120
	v_mfma_f32_16x16x4_f32 v[80:83], v113, v104, v[80:83]
	s_nop 9
	v_fma_f32 v80, v100, v112, v80
	v_fma_f32 v71, v100, v71, v81
	v_fma_f32 v81, v100, v105, v82
	v_fmac_f32_e32 v83, v100, v7
	v_mul_f32_e32 v7, 0x3d372713, v80
	v_mul_f32_e32 v82, 0x3d372713, v71
	v_mul_f32_e32 v105, 0x3d372713, v81
	v_mul_f32_e32 v112, 0x3d372713, v83
	v_mul_f32_e32 v7, v80, v7
	v_mul_f32_e32 v82, v71, v82
	v_mul_f32_e32 v105, v81, v105
	v_mul_f32_e32 v112, v83, v112
	v_fma_f32 v7, v80, v7, v80
	v_fma_f32 v82, v71, v82, v71
	v_fma_f32 v105, v81, v105, v81
	v_fma_f32 v112, v83, v112, v83
	v_mul_f32_e32 v7, 0xbfcc422a, v7
	v_mul_f32_e32 v82, 0xbfcc422a, v82
	v_mul_f32_e32 v105, 0xbfcc422a, v105
	v_mul_f32_e32 v112, 0xbfcc422a, v112
	v_mul_f32_e32 v7, 0x3fb8aa3b, v7
	v_mul_f32_e32 v82, 0x3fb8aa3b, v82
	v_mul_f32_e32 v105, 0x3fb8aa3b, v105
	v_mul_f32_e32 v112, 0x3fb8aa3b, v112
	v_exp_f32_e32 v7, v7
	v_exp_f32_e32 v82, v82
	v_exp_f32_e32 v105, v105
	v_exp_f32_e32 v112, v112
	v_add_f32_e32 v7, 1.0, v7
	v_add_f32_e32 v82, 1.0, v82
	v_add_f32_e32 v105, 1.0, v105
	v_add_f32_e32 v112, 1.0, v112
	v_rcp_f32_e32 v7, v7
	v_rcp_f32_e32 v82, v82
	v_rcp_f32_e32 v105, v105
	v_rcp_f32_e32 v112, v112
	v_mul_f32_e32 v7, v80, v7
	v_mul_f32_e32 v71, v71, v82
	v_mul_f32_e32 v80, v81, v105
	v_mul_f32_e32 v81, v83, v112
	v_bfe_u32 v82, v7, 16, 1
	global_store_dword v[106:107], v7, off
	v_bfe_u32 v83, v71, 16, 1
	v_bfe_u32 v105, v80, 16, 1
	v_bfe_u32 v106, v81, 16, 1
	v_add3_u32 v7, v7, v82, s96
	global_store_dword v[108:109], v71, off
	global_store_dword v[118:119], v80, off
	global_store_dword v[110:111], v81, off
	v_add3_u32 v71, v71, v83, s96
	v_add3_u32 v80, v80, v105, s96
	v_add3_u32 v81, v81, v106, s96
	global_store_short_d16_hi v[4:5], v7, off
	global_store_short_d16_hi v[10:11], v71, off
	global_store_short_d16_hi v[114:115], v80, off
	global_store_short_d16_hi v[116:117], v81, off
	s_cbranch_scc0 .LBB0_532
	v_lshrrev_b32_e32 v0, 3, v90
	v_and_b32_e32 v1, 7, v90
	v_lshl_add_u32 v0, v0, 2, v1
	v_add_u32_e32 v0, 0xa00, v0
	v_add_u32_e32 v2, 0x800, v90
	s_movk_i32 s0, 0x3ff
	v_cmp_lt_i32_e32 vcc, s0, v90
	v_cmp_lt_u32_e64 s[0:1], 3, v1
	s_nop 1
	v_cndmask_b32_e32 v0, v2, v0, vcc
	s_and_b64 s[0:1], s[0:1], vcc
	s_movk_i32 s2, 0x7ff
	v_cmp_lt_i32_e32 vcc, s2, v90
	s_nop 1
	s_or_b64 vcc, vcc, s[0:1]
	s_or_b64 s[26:27], vcc, s[26:27]
	v_mov_b32_e32 v90, v0
	s_andn2_b64 exec, exec, s[26:27]
	s_cbranch_execnz .LBB0_519
